# v16 + grid barrier: non-leader workgroups spin on the top generation word directly (one hop fewer on the release path)
# speedup vs baseline: 1.0160x; 1.0010x over previous
.LBB0_92:
	s_or_b64 exec, exec, s[8:9]
	v_cvt_f32_u32_e32 v5, v3
	s_waitcnt vmcnt(0)
	v_readfirstlane_b32 s6, v4
	v_sub_u32_e32 v4, 0, v3
	v_rcp_iflag_f32_e32 v5, v5
	v_add_u32_e32 v6, s6, v2
	v_mul_f32_e32 v5, 0x4f7ffffe, v5
	v_cvt_u32_f32_e32 v5, v5
	v_mul_lo_u32 v2, v4, v5
	v_mul_hi_u32 v2, v5, v2
	v_add_u32_e32 v2, v5, v2
	v_mul_hi_u32 v2, v6, v2
	v_mul_lo_u32 v4, v2, v3
	v_sub_u32_e32 v4, v6, v4
	v_add_u32_e32 v5, 1, v2
	v_cmp_ge_u32_e32 vcc, v4, v3
	s_nop 1
	v_cndmask_b32_e32 v2, v2, v5, vcc
	v_sub_u32_e32 v5, v4, v3
	v_cndmask_b32_e32 v4, v4, v5, vcc
	v_add_u32_e32 v5, 1, v2
	v_cmp_ge_u32_e32 vcc, v4, v3
	v_add_u32_e32 v4, 1, v6
	s_nop 0
	v_cndmask_b32_e32 v2, v2, v5, vcc
	v_mul_lo_u32 v5, v3, v2
	v_add_u32_e32 v3, v5, v3
	v_cmp_ne_u32_e32 vcc, v4, v3
	s_and_saveexec_b64 s[6:7], vcc
	s_xor_b64 s[6:7], exec, s[6:7]
	s_cbranch_execz .LBB0_106
	s_waitcnt lgkmcnt(0)
	v_mov_b32_e32 v1, 0x7100
	global_load_dword v1, v1, s[50:51] offset:1024 sc1
	s_add_u32 s12, s50, 0x7500
	s_addc_u32 s13, s51, 0
	s_waitcnt vmcnt(0)
	v_cmp_eq_u32_e32 vcc, v1, v2
	s_and_saveexec_b64 s[8:9], vcc
	s_cbranch_execz .LBB0_105
	s_add_u32 s10, s50, 0x4200
	s_addc_u32 s11, s51, 0
	s_mov_b32 s24, 1
	s_mov_b64 s[14:15], 0
	v_mov_b32_e32 v1, 0
	s_branch .LBB0_96

.LBB0_2025:
	s_or_b64 exec, exec, s[8:9]
	v_cvt_f32_u32_e32 v4, v2
	s_waitcnt vmcnt(0)
	v_readfirstlane_b32 s6, v3
	v_sub_u32_e32 v3, 0, v2
	v_rcp_iflag_f32_e32 v4, v4
	v_add_u32_e32 v5, s6, v1
	v_mul_f32_e32 v4, 0x4f7ffffe, v4
	v_cvt_u32_f32_e32 v4, v4
	v_mul_lo_u32 v1, v3, v4
	v_mul_hi_u32 v1, v4, v1
	v_add_u32_e32 v1, v4, v1
	v_mul_hi_u32 v1, v5, v1
	v_mul_lo_u32 v3, v1, v2
	v_sub_u32_e32 v3, v5, v3
	v_add_u32_e32 v4, 1, v1
	v_cmp_ge_u32_e32 vcc, v3, v2
	s_nop 1
	v_cndmask_b32_e32 v1, v1, v4, vcc
	v_sub_u32_e32 v4, v3, v2
	v_cndmask_b32_e32 v3, v3, v4, vcc
	v_add_u32_e32 v4, 1, v1
	v_cmp_ge_u32_e32 vcc, v3, v2
	v_add_u32_e32 v3, 1, v5
	s_nop 0
	v_cndmask_b32_e32 v1, v1, v4, vcc
	v_mul_lo_u32 v4, v2, v1
	v_add_u32_e32 v2, v4, v2
	v_cmp_ne_u32_e32 vcc, v3, v2
	s_and_saveexec_b64 s[6:7], vcc
	s_xor_b64 s[6:7], exec, s[6:7]
	s_cbranch_execz .LBB0_2039
	s_waitcnt lgkmcnt(0)
	v_mov_b32_e32 v0, 0x7100
	global_load_dword v0, v0, s[50:51] offset:1024 sc1
	s_add_u32 s12, s50, 0x7500
	s_addc_u32 s13, s51, 0
	s_waitcnt vmcnt(0)
	v_cmp_eq_u32_e32 vcc, v0, v1
	s_and_saveexec_b64 s[8:9], vcc
	s_cbranch_execz .LBB0_2038
	s_add_u32 s10, s50, 0x4200
	s_addc_u32 s11, s51, 0
	s_mov_b32 s24, 1
	s_mov_b64 s[14:15], 0
	v_mov_b32_e32 v0, 0
	s_branch .LBB0_2029
